# v83 plus cmp-attn distance-table build rewritten: constant regions filled with ds_write_b128, only the 792 near distances per head looked up, batched (no per-entry division / visibility branch / LDS r
# speedup vs baseline: 1.0075x; 1.0010x over previous
.LBB0_868:
	v_readfirstlane_b32 s6, v138
	s_lshr_b32 s6, s6, 7
	v_and_b32_e32 v90, 0x7f, v138
	s_mul_i32 s7, s6, 0x2ca0
	s_add_i32 s7, s7, 0x14400
	s_lshl_b32 s20, s6, 2
	s_add_i32 s20, s20, s8
	s_add_i32 s21, s7, 0x1020
	s_add_i32 s28, s7, 0x1c80
	v_mov_b32_e32 v91, s20
	ds_read_b32 v91, v91 offset:1984
	v_mov_b32_e32 v104, v90
	v_sub_u32_e32 v125, 0x317, v104
	v_cvt_f32_u32_e32 v126, v125
	v_log_f32_e32 v126, v126
	v_cmp_gt_u32_e32 vcc, 16, v125
	v_mul_f32_e32 v126, 0x402aaaab, v126
	v_add_f32_e32 v126, 0x40aaab7c, v126
	v_cvt_u32_f32_e32 v126, v126
	v_min_u32_e32 v126, 31, v126
	v_cndmask_b32_e32 v126, v126, v125, vcc
	v_lshl_add_u32 v127, v126, 6, s20
	ds_read_b32 v111, v127
	v_lshl_add_u32 v118, v104, 2, s21
	v_add_u32_e32 v105, 0x80, v90
	v_sub_u32_e32 v125, 0x317, v105
	v_cvt_f32_u32_e32 v126, v125
	v_log_f32_e32 v126, v126
	v_cmp_gt_u32_e32 vcc, 16, v125
	v_mul_f32_e32 v126, 0x402aaaab, v126
	v_add_f32_e32 v126, 0x40aaab7c, v126
	v_cvt_u32_f32_e32 v126, v126
	v_min_u32_e32 v126, 31, v126
	v_cndmask_b32_e32 v126, v126, v125, vcc
	v_lshl_add_u32 v127, v126, 6, s20
	ds_read_b32 v112, v127
	v_lshl_add_u32 v119, v105, 2, s21
	v_add_u32_e32 v106, 0x100, v90
	v_sub_u32_e32 v125, 0x317, v106
	v_cvt_f32_u32_e32 v126, v125
	v_log_f32_e32 v126, v126
	v_cmp_gt_u32_e32 vcc, 16, v125
	v_mul_f32_e32 v126, 0x402aaaab, v126
	v_add_f32_e32 v126, 0x40aaab7c, v126
	v_cvt_u32_f32_e32 v126, v126
	v_min_u32_e32 v126, 31, v126
	v_cndmask_b32_e32 v126, v126, v125, vcc
	v_lshl_add_u32 v127, v126, 6, s20
	ds_read_b32 v113, v127
	v_lshl_add_u32 v120, v106, 2, s21
	v_add_u32_e32 v107, 0x180, v90
	v_sub_u32_e32 v125, 0x317, v107
	v_cvt_f32_u32_e32 v126, v125
	v_log_f32_e32 v126, v126
	v_cmp_gt_u32_e32 vcc, 16, v125
	v_mul_f32_e32 v126, 0x402aaaab, v126
	v_add_f32_e32 v126, 0x40aaab7c, v126
	v_cvt_u32_f32_e32 v126, v126
	v_min_u32_e32 v126, 31, v126
	v_cndmask_b32_e32 v126, v126, v125, vcc
	v_lshl_add_u32 v127, v126, 6, s20
	ds_read_b32 v114, v127
	v_lshl_add_u32 v121, v107, 2, s21
	v_add_u32_e32 v108, 0x200, v90
	v_sub_u32_e32 v125, 0x317, v108
	v_cvt_f32_u32_e32 v126, v125
	v_log_f32_e32 v126, v126
	v_cmp_gt_u32_e32 vcc, 16, v125
	v_mul_f32_e32 v126, 0x402aaaab, v126
	v_add_f32_e32 v126, 0x40aaab7c, v126
	v_cvt_u32_f32_e32 v126, v126
	v_min_u32_e32 v126, 31, v126
	v_cndmask_b32_e32 v126, v126, v125, vcc
	v_lshl_add_u32 v127, v126, 6, s20
	ds_read_b32 v115, v127
	v_lshl_add_u32 v122, v108, 2, s21
	v_add_u32_e32 v109, 0x280, v90
	v_sub_u32_e32 v125, 0x317, v109
	v_cvt_f32_u32_e32 v126, v125
	v_log_f32_e32 v126, v126
	v_cmp_gt_u32_e32 vcc, 16, v125
	v_mul_f32_e32 v126, 0x402aaaab, v126
	v_add_f32_e32 v126, 0x40aaab7c, v126
	v_cvt_u32_f32_e32 v126, v126
	v_min_u32_e32 v126, 31, v126
	v_cndmask_b32_e32 v126, v126, v125, vcc
	v_lshl_add_u32 v127, v126, 6, s20
	ds_read_b32 v116, v127
	v_lshl_add_u32 v123, v109, 2, s21
	v_add_u32_e32 v110, 0x300, v90
	v_min_u32_e32 v110, 0x317, v110
	v_sub_u32_e32 v125, 0x317, v110
	v_cvt_f32_u32_e32 v126, v125
	v_log_f32_e32 v126, v126
	v_cmp_gt_u32_e32 vcc, 16, v125
	v_mul_f32_e32 v126, 0x402aaaab, v126
	v_add_f32_e32 v126, 0x40aaab7c, v126
	v_cvt_u32_f32_e32 v126, v126
	v_min_u32_e32 v126, 31, v126
	v_cndmask_b32_e32 v126, v126, v125, vcc
	v_lshl_add_u32 v127, v126, 6, s20
	ds_read_b32 v117, v127
	v_lshl_add_u32 v124, v110, 2, s21
	s_waitcnt lgkmcnt(7)
	v_mov_b32_e32 v96, v91
	v_mov_b32_e32 v97, v91
	v_mov_b32_e32 v98, v91
	v_mov_b32_e32 v99, v91
	v_mov_b32_e32 v100, 0xf149f2ca
	v_mov_b32_e32 v101, 0xf149f2ca
	v_mov_b32_e32 v102, 0xf149f2ca
	v_mov_b32_e32 v103, 0xf149f2ca
	v_lshl_add_u32 v128, v90, 4, s7
	v_lshl_add_u32 v129, v90, 4, s28
	ds_write_b128 v128, v[96:99]
	ds_write_b128 v129, v[100:103]
	v_add_u32_e32 v130, 0x80, v90
	v_lshl_add_u32 v128, v130, 4, s7
	v_lshl_add_u32 v129, v130, 4, s28
	ds_write_b128 v128, v[96:99]
	ds_write_b128 v129, v[100:103]
	v_add_u32_e32 v130, 0x100, v90
	v_min_u32_e32 v130, 0x101, v130
	v_lshl_add_u32 v128, v130, 4, s7
	v_lshl_add_u32 v129, v130, 4, s28
	ds_write_b128 v128, v[96:99]
	ds_write_b128 v129, v[100:103]
	s_waitcnt lgkmcnt(0)
	ds_write_b32 v118, v111
	ds_write_b32 v119, v112
	ds_write_b32 v120, v113
	ds_write_b32 v121, v114
	ds_write_b32 v122, v115
	ds_write_b32 v123, v116
	ds_write_b32 v124, v117
